# v43 + lever 7.3: fp8 GEMM epilogues of P7/P9a/P15 store 16 B per lane (pairs of 8-B row stores merged through v_permlane16_swap)
# speedup vs baseline: 1.0072x; 1.0018x over previous
.LBB0_677:
	v_mbcnt_lo_u32_b32 v250, -1, 0
	v_mbcnt_hi_u32_b32 v250, -1, v250
	v_bfe_u32 v250, v250, 4, 1
	v_mul_u32_u24_e32 v250, 0x78, v250
	v_mov_b32_e32 v251, 0
	s_lshl_b32 s27, s81, 10
	s_and_b32 s27, s27, 0x400
	v_mov_b32_e32 v17, v171
	v_mov_b32_e32 v16, v204
	s_add_i32 s27, s67, s27
	s_and_b64 vcc, exec, s[2:3]
	v_lshl_add_u32 v0, v16, 5, s27
	s_lshl_b32 s27, s80, 8
	s_or_b32 s27, s27, s66
	ds_read_b128 v[12:15], v0
	ds_read_b128 v[8:11], v0 offset:16
	ds_read_b128 v[4:7], v0 offset:512
	ds_read_b128 v[0:3], v0 offset:528
	v_lshl_add_u32 v16, v16, 3, s27
	s_lshl_b32 s27, s79, 8
	s_add_i32 s27, s27, s68
	v_add_u32_e32 v18, s27, v17
	s_waitcnt lgkmcnt(0)
	v_pk_fma_f32 v[22:23], v[158:159], s[22:23], v[14:15] op_sel_hi:[1,0,1]
	v_pk_fma_f32 v[24:25], v[156:157], s[22:23], v[12:13] op_sel_hi:[1,0,1]
	v_ashrrev_i32_e32 v19, 31, v18
	v_pk_mul_f32 v[22:23], v[22:23], s[24:25] op_sel_hi:[1,0]
	v_pk_mul_f32 v[24:25], v[24:25], s[24:25] op_sel_hi:[1,0]
	v_pk_fma_f32 v[28:29], v[152:153], s[22:23], v[8:9] op_sel_hi:[1,0,1]
	v_lshlrev_b64 v[20:21], 10, v[18:19]
	v_pk_mul_f32 v[28:29], v[28:29], s[24:25] op_sel_hi:[1,0]
	v_med3_f32 v19, v24, s75, v210
	v_med3_f32 v24, v25, s75, v210
	v_med3_f32 v25, v22, s75, v210
	v_mov_b32_e32 v22, v165
	v_med3_f32 v30, v23, s75, v210
	v_cvt_pk_fp8_f32 v22, v19, v24
	v_med3_f32 v19, v28, s75, v210
	v_med3_f32 v24, v29, s75, v210
	v_mov_b32_e32 v23, v165
	v_cvt_pk_fp8_f32 v23, v19, v24
	v_pk_fma_f32 v[26:27], v[154:155], s[22:23], v[10:11] op_sel_hi:[1,0,1]
	v_cvt_pk_fp8_f32 v22, v25, v30 op_sel:[0,0,1]
	v_pk_mul_f32 v[26:27], v[26:27], s[24:25] op_sel_hi:[1,0]
	v_pk_fma_f32 v[30:31], v[144:145], s[22:23], v[0:1] op_sel_hi:[1,0,1]
	v_med3_f32 v19, v26, s75, v210
	v_med3_f32 v24, v27, s75, v210
	v_cvt_pk_fp8_f32 v23, v19, v24 op_sel:[0,0,1]
	v_pk_fma_f32 v[24:25], v[150:151], s[22:23], v[6:7] op_sel_hi:[1,0,1]
	v_pk_fma_f32 v[26:27], v[148:149], s[22:23], v[4:5] op_sel_hi:[1,0,1]
	v_pk_mul_f32 v[24:25], v[24:25], s[24:25] op_sel_hi:[1,0]
	v_pk_mul_f32 v[26:27], v[26:27], s[24:25] op_sel_hi:[1,0]
	v_pk_mul_f32 v[30:31], v[30:31], s[24:25] op_sel_hi:[1,0]
	v_med3_f32 v19, v26, s75, v210
	v_med3_f32 v26, v27, s75, v210
	v_med3_f32 v27, v24, s75, v210
	v_mov_b32_e32 v24, v165
	v_med3_f32 v144, v25, s75, v210
	v_cvt_pk_fp8_f32 v24, v19, v26
	v_med3_f32 v19, v30, s75, v210
	v_med3_f32 v26, v31, s75, v210
	v_mov_b32_e32 v25, v165
	v_cvt_pk_fp8_f32 v25, v19, v26
	v_pk_fma_f32 v[28:29], v[146:147], s[22:23], v[2:3] op_sel_hi:[1,0,1]
	v_cvt_pk_fp8_f32 v24, v27, v144 op_sel:[0,0,1]
	v_pk_mul_f32 v[28:29], v[28:29], s[24:25] op_sel_hi:[1,0]
	v_ashrrev_i32_e32 v17, 31, v16
	v_med3_f32 v19, v28, s75, v210
	v_med3_f32 v26, v29, s75, v210
	v_cvt_pk_fp8_f32 v25, v19, v26 op_sel:[0,0,1]
	v_lshl_add_u64 v[20:21], s[12:13], 0, v[20:21]
	v_lshl_add_u64 v[20:21], v[20:21], 0, v[16:17]
	s_nop 1
	v_permlane16_swap_b32_e32 v22, v24
	v_permlane16_swap_b32_e32 v23, v25
	v_lshl_add_u64 v[248:249], v[20:21], 0, v[250:251]
	global_store_dwordx4 v[248:249], v[22:25], off
	s_nop 1
	v_pk_fma_f32 v[22:23], v[142:143], s[22:23], v[14:15] op_sel_hi:[1,0,1]
	v_pk_fma_f32 v[24:25], v[140:141], s[22:23], v[12:13] op_sel_hi:[1,0,1]
	v_pk_mul_f32 v[22:23], v[22:23], s[24:25] op_sel_hi:[1,0]
	v_pk_mul_f32 v[24:25], v[24:25], s[24:25] op_sel_hi:[1,0]
	v_pk_fma_f32 v[28:29], v[136:137], s[22:23], v[8:9] op_sel_hi:[1,0,1]
	v_med3_f32 v19, v24, s75, v210
	v_pk_mul_f32 v[28:29], v[28:29], s[24:25] op_sel_hi:[1,0]
	v_med3_f32 v24, v25, s75, v210
	v_med3_f32 v25, v22, s75, v210
	v_mov_b32_e32 v22, v165
	v_med3_f32 v30, v23, s75, v210
	v_cvt_pk_fp8_f32 v22, v19, v24
	v_med3_f32 v19, v28, s75, v210
	v_med3_f32 v24, v29, s75, v210
	v_mov_b32_e32 v23, v165
	v_cvt_pk_fp8_f32 v23, v19, v24
	v_pk_fma_f32 v[26:27], v[138:139], s[22:23], v[10:11] op_sel_hi:[1,0,1]
	v_cvt_pk_fp8_f32 v22, v25, v30 op_sel:[0,0,1]
	v_pk_mul_f32 v[26:27], v[26:27], s[24:25] op_sel_hi:[1,0]
	v_pk_fma_f32 v[30:31], v[128:129], s[22:23], v[0:1] op_sel_hi:[1,0,1]
	v_med3_f32 v19, v26, s75, v210
	v_med3_f32 v24, v27, s75, v210
	v_cvt_pk_fp8_f32 v23, v19, v24 op_sel:[0,0,1]
	v_pk_fma_f32 v[24:25], v[134:135], s[22:23], v[6:7] op_sel_hi:[1,0,1]
	v_pk_fma_f32 v[26:27], v[132:133], s[22:23], v[4:5] op_sel_hi:[1,0,1]
	v_pk_mul_f32 v[24:25], v[24:25], s[24:25] op_sel_hi:[1,0]
	v_pk_mul_f32 v[26:27], v[26:27], s[24:25] op_sel_hi:[1,0]
	v_pk_mul_f32 v[30:31], v[30:31], s[24:25] op_sel_hi:[1,0]
	v_med3_f32 v19, v26, s75, v210
	v_med3_f32 v26, v27, s75, v210
	v_med3_f32 v27, v24, s75, v210
	v_mov_b32_e32 v24, v165
	v_med3_f32 v128, v25, s75, v210
	v_cvt_pk_fp8_f32 v24, v19, v26
	v_med3_f32 v19, v30, s75, v210
	v_med3_f32 v26, v31, s75, v210
	v_mov_b32_e32 v25, v165
	v_cvt_pk_fp8_f32 v25, v19, v26
	v_pk_fma_f32 v[28:29], v[130:131], s[22:23], v[2:3] op_sel_hi:[1,0,1]
	v_add_u32_e32 v20, 16, v18
	v_pk_mul_f32 v[28:29], v[28:29], s[24:25] op_sel_hi:[1,0]
	v_ashrrev_i32_e32 v21, 31, v20
	v_med3_f32 v19, v28, s75, v210
	v_med3_f32 v26, v29, s75, v210
	v_lshlrev_b64 v[20:21], 10, v[20:21]
	v_cvt_pk_fp8_f32 v24, v27, v128 op_sel:[0,0,1]
	v_cvt_pk_fp8_f32 v25, v19, v26 op_sel:[0,0,1]
	v_lshl_add_u64 v[20:21], s[12:13], 0, v[20:21]
	v_lshl_add_u64 v[20:21], v[20:21], 0, v[16:17]
	s_nop 1
	v_permlane16_swap_b32_e32 v22, v24
	v_permlane16_swap_b32_e32 v23, v25
	v_lshl_add_u64 v[248:249], v[20:21], 0, v[250:251]
	global_store_dwordx4 v[248:249], v[22:25], off
	s_nop 1
	v_pk_fma_f32 v[22:23], v[126:127], s[22:23], v[14:15] op_sel_hi:[1,0,1]
	v_pk_fma_f32 v[24:25], v[124:125], s[22:23], v[12:13] op_sel_hi:[1,0,1]
	v_pk_mul_f32 v[22:23], v[22:23], s[24:25] op_sel_hi:[1,0]
	v_pk_mul_f32 v[24:25], v[24:25], s[24:25] op_sel_hi:[1,0]
	v_pk_fma_f32 v[28:29], v[120:121], s[22:23], v[8:9] op_sel_hi:[1,0,1]
	v_med3_f32 v19, v24, s75, v210
	v_pk_mul_f32 v[28:29], v[28:29], s[24:25] op_sel_hi:[1,0]
	v_med3_f32 v24, v25, s75, v210
	v_med3_f32 v25, v22, s75, v210
	v_mov_b32_e32 v22, v165
	v_med3_f32 v30, v23, s75, v210
	v_cvt_pk_fp8_f32 v22, v19, v24
	v_med3_f32 v19, v28, s75, v210
	v_med3_f32 v24, v29, s75, v210
	v_mov_b32_e32 v23, v165
	v_cvt_pk_fp8_f32 v23, v19, v24
	v_pk_fma_f32 v[26:27], v[122:123], s[22:23], v[10:11] op_sel_hi:[1,0,1]
	v_cvt_pk_fp8_f32 v22, v25, v30 op_sel:[0,0,1]
	v_pk_mul_f32 v[26:27], v[26:27], s[24:25] op_sel_hi:[1,0]
	v_pk_fma_f32 v[30:31], v[112:113], s[22:23], v[0:1] op_sel_hi:[1,0,1]
	v_med3_f32 v19, v26, s75, v210
	v_med3_f32 v24, v27, s75, v210
	v_cvt_pk_fp8_f32 v23, v19, v24 op_sel:[0,0,1]
	v_pk_fma_f32 v[24:25], v[118:119], s[22:23], v[6:7] op_sel_hi:[1,0,1]
	v_pk_fma_f32 v[26:27], v[116:117], s[22:23], v[4:5] op_sel_hi:[1,0,1]
	v_pk_mul_f32 v[24:25], v[24:25], s[24:25] op_sel_hi:[1,0]
	v_pk_mul_f32 v[26:27], v[26:27], s[24:25] op_sel_hi:[1,0]
	v_pk_mul_f32 v[30:31], v[30:31], s[24:25] op_sel_hi:[1,0]
	v_med3_f32 v19, v26, s75, v210
	v_med3_f32 v26, v27, s75, v210
	v_med3_f32 v27, v24, s75, v210
	v_mov_b32_e32 v24, v165
	v_med3_f32 v112, v25, s75, v210
	v_cvt_pk_fp8_f32 v24, v19, v26
	v_med3_f32 v19, v30, s75, v210
	v_med3_f32 v26, v31, s75, v210
	v_mov_b32_e32 v25, v165
	v_cvt_pk_fp8_f32 v25, v19, v26
	v_pk_fma_f32 v[28:29], v[114:115], s[22:23], v[2:3] op_sel_hi:[1,0,1]
	v_add_u32_e32 v20, 32, v18
	v_pk_mul_f32 v[28:29], v[28:29], s[24:25] op_sel_hi:[1,0]
	v_ashrrev_i32_e32 v21, 31, v20
	v_med3_f32 v19, v28, s75, v210
	v_med3_f32 v26, v29, s75, v210
	v_lshlrev_b64 v[20:21], 10, v[20:21]
	v_cvt_pk_fp8_f32 v24, v27, v112 op_sel:[0,0,1]
	v_cvt_pk_fp8_f32 v25, v19, v26 op_sel:[0,0,1]
	v_lshl_add_u64 v[20:21], s[12:13], 0, v[20:21]
	v_lshl_add_u64 v[20:21], v[20:21], 0, v[16:17]
	s_nop 1
	v_permlane16_swap_b32_e32 v22, v24
	v_permlane16_swap_b32_e32 v23, v25
	v_lshl_add_u64 v[248:249], v[20:21], 0, v[250:251]
	global_store_dwordx4 v[248:249], v[22:25], off
	s_nop 1
	v_pk_fma_f32 v[22:23], v[110:111], s[22:23], v[14:15] op_sel_hi:[1,0,1]
	v_pk_fma_f32 v[24:25], v[108:109], s[22:23], v[12:13] op_sel_hi:[1,0,1]
	v_pk_mul_f32 v[22:23], v[22:23], s[24:25] op_sel_hi:[1,0]
	v_pk_mul_f32 v[24:25], v[24:25], s[24:25] op_sel_hi:[1,0]
	v_pk_fma_f32 v[28:29], v[104:105], s[22:23], v[8:9] op_sel_hi:[1,0,1]
	v_med3_f32 v19, v24, s75, v210
	v_pk_mul_f32 v[28:29], v[28:29], s[24:25] op_sel_hi:[1,0]
	v_med3_f32 v24, v25, s75, v210
	v_med3_f32 v25, v22, s75, v210
	v_mov_b32_e32 v22, v165
	v_med3_f32 v30, v23, s75, v210
	v_cvt_pk_fp8_f32 v22, v19, v24
	v_med3_f32 v19, v28, s75, v210
	v_med3_f32 v24, v29, s75, v210
	v_mov_b32_e32 v23, v165
	v_cvt_pk_fp8_f32 v23, v19, v24
	v_pk_fma_f32 v[26:27], v[106:107], s[22:23], v[10:11] op_sel_hi:[1,0,1]
	v_cvt_pk_fp8_f32 v22, v25, v30 op_sel:[0,0,1]
	v_pk_mul_f32 v[26:27], v[26:27], s[24:25] op_sel_hi:[1,0]
	v_pk_fma_f32 v[30:31], v[96:97], s[22:23], v[0:1] op_sel_hi:[1,0,1]
	v_med3_f32 v19, v26, s75, v210
	v_med3_f32 v24, v27, s75, v210
	v_cvt_pk_fp8_f32 v23, v19, v24 op_sel:[0,0,1]
	v_pk_fma_f32 v[24:25], v[102:103], s[22:23], v[6:7] op_sel_hi:[1,0,1]
	v_pk_fma_f32 v[26:27], v[100:101], s[22:23], v[4:5] op_sel_hi:[1,0,1]
	v_pk_mul_f32 v[24:25], v[24:25], s[24:25] op_sel_hi:[1,0]
	v_pk_mul_f32 v[26:27], v[26:27], s[24:25] op_sel_hi:[1,0]
	v_pk_mul_f32 v[30:31], v[30:31], s[24:25] op_sel_hi:[1,0]
	v_med3_f32 v19, v26, s75, v210
	v_med3_f32 v26, v27, s75, v210
	v_med3_f32 v27, v24, s75, v210
	v_mov_b32_e32 v24, v165
	v_med3_f32 v96, v25, s75, v210
	v_cvt_pk_fp8_f32 v24, v19, v26
	v_med3_f32 v19, v30, s75, v210
	v_med3_f32 v26, v31, s75, v210
	v_mov_b32_e32 v25, v165
	v_cvt_pk_fp8_f32 v25, v19, v26
	v_pk_fma_f32 v[28:29], v[98:99], s[22:23], v[2:3] op_sel_hi:[1,0,1]
	v_add_u32_e32 v20, 48, v18
	v_pk_mul_f32 v[28:29], v[28:29], s[24:25] op_sel_hi:[1,0]
	v_ashrrev_i32_e32 v21, 31, v20
	v_med3_f32 v19, v28, s75, v210
	v_med3_f32 v26, v29, s75, v210
	v_lshlrev_b64 v[20:21], 10, v[20:21]
	v_cvt_pk_fp8_f32 v24, v27, v96 op_sel:[0,0,1]
	v_cvt_pk_fp8_f32 v25, v19, v26 op_sel:[0,0,1]
	v_lshl_add_u64 v[20:21], s[12:13], 0, v[20:21]
	v_lshl_add_u64 v[20:21], v[20:21], 0, v[16:17]
	s_nop 1
	v_permlane16_swap_b32_e32 v22, v24
	v_permlane16_swap_b32_e32 v23, v25
	v_lshl_add_u64 v[248:249], v[20:21], 0, v[250:251]
	global_store_dwordx4 v[248:249], v[22:25], off
	s_nop 1
	v_pk_fma_f32 v[22:23], v[94:95], s[22:23], v[14:15] op_sel_hi:[1,0,1]
	v_pk_fma_f32 v[24:25], v[92:93], s[22:23], v[12:13] op_sel_hi:[1,0,1]
	v_pk_mul_f32 v[22:23], v[22:23], s[24:25] op_sel_hi:[1,0]
	v_pk_mul_f32 v[24:25], v[24:25], s[24:25] op_sel_hi:[1,0]
	v_pk_fma_f32 v[28:29], v[88:89], s[22:23], v[8:9] op_sel_hi:[1,0,1]
	v_med3_f32 v19, v24, s75, v210
	v_pk_mul_f32 v[28:29], v[28:29], s[24:25] op_sel_hi:[1,0]
	v_med3_f32 v24, v25, s75, v210
	v_med3_f32 v25, v22, s75, v210
	v_mov_b32_e32 v22, v165
	v_med3_f32 v30, v23, s75, v210
	v_cvt_pk_fp8_f32 v22, v19, v24
	v_med3_f32 v19, v28, s75, v210
	v_med3_f32 v24, v29, s75, v210
	v_mov_b32_e32 v23, v165
	v_cvt_pk_fp8_f32 v23, v19, v24
	v_pk_fma_f32 v[26:27], v[90:91], s[22:23], v[10:11] op_sel_hi:[1,0,1]
	v_cvt_pk_fp8_f32 v22, v25, v30 op_sel:[0,0,1]
	v_pk_mul_f32 v[26:27], v[26:27], s[24:25] op_sel_hi:[1,0]
	v_pk_fma_f32 v[30:31], v[80:81], s[22:23], v[0:1] op_sel_hi:[1,0,1]
	v_med3_f32 v19, v26, s75, v210
	v_med3_f32 v24, v27, s75, v210
	v_cvt_pk_fp8_f32 v23, v19, v24 op_sel:[0,0,1]
	v_pk_fma_f32 v[24:25], v[86:87], s[22:23], v[6:7] op_sel_hi:[1,0,1]
	v_pk_fma_f32 v[26:27], v[84:85], s[22:23], v[4:5] op_sel_hi:[1,0,1]
	v_pk_mul_f32 v[24:25], v[24:25], s[24:25] op_sel_hi:[1,0]
	v_pk_mul_f32 v[26:27], v[26:27], s[24:25] op_sel_hi:[1,0]
	v_pk_mul_f32 v[30:31], v[30:31], s[24:25] op_sel_hi:[1,0]
	v_med3_f32 v19, v26, s75, v210
	v_med3_f32 v26, v27, s75, v210
	v_med3_f32 v27, v24, s75, v210
	v_mov_b32_e32 v24, v165
	v_med3_f32 v80, v25, s75, v210
	v_cvt_pk_fp8_f32 v24, v19, v26
	v_med3_f32 v19, v30, s75, v210
	v_med3_f32 v26, v31, s75, v210
	v_mov_b32_e32 v25, v165
	v_cvt_pk_fp8_f32 v25, v19, v26
	v_pk_fma_f32 v[28:29], v[82:83], s[22:23], v[2:3] op_sel_hi:[1,0,1]
	v_add_u32_e32 v20, 0x80, v18
	v_pk_mul_f32 v[28:29], v[28:29], s[24:25] op_sel_hi:[1,0]
	v_ashrrev_i32_e32 v21, 31, v20
	v_med3_f32 v19, v28, s75, v210
	v_med3_f32 v26, v29, s75, v210
	v_lshlrev_b64 v[20:21], 10, v[20:21]
	v_cvt_pk_fp8_f32 v24, v27, v80 op_sel:[0,0,1]
	v_cvt_pk_fp8_f32 v25, v19, v26 op_sel:[0,0,1]
	v_lshl_add_u64 v[20:21], s[12:13], 0, v[20:21]
	v_lshl_add_u64 v[20:21], v[20:21], 0, v[16:17]
	s_nop 1
	v_permlane16_swap_b32_e32 v22, v24
	v_permlane16_swap_b32_e32 v23, v25
	v_lshl_add_u64 v[248:249], v[20:21], 0, v[250:251]
	global_store_dwordx4 v[248:249], v[22:25], off
	s_nop 1
	v_pk_fma_f32 v[22:23], v[78:79], s[22:23], v[14:15] op_sel_hi:[1,0,1]
	v_pk_fma_f32 v[24:25], v[76:77], s[22:23], v[12:13] op_sel_hi:[1,0,1]
	v_pk_mul_f32 v[22:23], v[22:23], s[24:25] op_sel_hi:[1,0]
	v_pk_mul_f32 v[24:25], v[24:25], s[24:25] op_sel_hi:[1,0]
	v_pk_fma_f32 v[28:29], v[72:73], s[22:23], v[8:9] op_sel_hi:[1,0,1]
	v_med3_f32 v19, v24, s75, v210
	v_pk_mul_f32 v[28:29], v[28:29], s[24:25] op_sel_hi:[1,0]
	v_med3_f32 v24, v25, s75, v210
	v_med3_f32 v25, v22, s75, v210
	v_mov_b32_e32 v22, v165
	v_med3_f32 v30, v23, s75, v210
	v_cvt_pk_fp8_f32 v22, v19, v24
	v_med3_f32 v19, v28, s75, v210
	v_med3_f32 v24, v29, s75, v210
	v_mov_b32_e32 v23, v165
	v_cvt_pk_fp8_f32 v23, v19, v24
	v_pk_fma_f32 v[26:27], v[74:75], s[22:23], v[10:11] op_sel_hi:[1,0,1]
	v_cvt_pk_fp8_f32 v22, v25, v30 op_sel:[0,0,1]
	v_pk_mul_f32 v[26:27], v[26:27], s[24:25] op_sel_hi:[1,0]
	v_pk_fma_f32 v[30:31], v[64:65], s[22:23], v[0:1] op_sel_hi:[1,0,1]
	v_med3_f32 v19, v26, s75, v210
	v_med3_f32 v24, v27, s75, v210
	v_cvt_pk_fp8_f32 v23, v19, v24 op_sel:[0,0,1]
	v_pk_fma_f32 v[24:25], v[70:71], s[22:23], v[6:7] op_sel_hi:[1,0,1]
	v_pk_fma_f32 v[26:27], v[68:69], s[22:23], v[4:5] op_sel_hi:[1,0,1]
	v_pk_mul_f32 v[24:25], v[24:25], s[24:25] op_sel_hi:[1,0]
	v_pk_mul_f32 v[26:27], v[26:27], s[24:25] op_sel_hi:[1,0]
	v_pk_mul_f32 v[30:31], v[30:31], s[24:25] op_sel_hi:[1,0]
	v_med3_f32 v19, v26, s75, v210
	v_med3_f32 v26, v27, s75, v210
	v_med3_f32 v27, v24, s75, v210
	v_mov_b32_e32 v24, v165
	v_med3_f32 v64, v25, s75, v210
	v_cvt_pk_fp8_f32 v24, v19, v26
	v_med3_f32 v19, v30, s75, v210
	v_med3_f32 v26, v31, s75, v210
	v_mov_b32_e32 v25, v165
	v_cvt_pk_fp8_f32 v25, v19, v26
	v_pk_fma_f32 v[28:29], v[66:67], s[22:23], v[2:3] op_sel_hi:[1,0,1]
	v_add_u32_e32 v20, 0x90, v18
	v_pk_mul_f32 v[28:29], v[28:29], s[24:25] op_sel_hi:[1,0]
	v_ashrrev_i32_e32 v21, 31, v20
	v_med3_f32 v19, v28, s75, v210
	v_med3_f32 v26, v29, s75, v210
	v_lshlrev_b64 v[20:21], 10, v[20:21]
	v_cvt_pk_fp8_f32 v24, v27, v64 op_sel:[0,0,1]
	v_cvt_pk_fp8_f32 v25, v19, v26 op_sel:[0,0,1]
	v_lshl_add_u64 v[20:21], s[12:13], 0, v[20:21]
	v_lshl_add_u64 v[20:21], v[20:21], 0, v[16:17]
	s_nop 1
	v_permlane16_swap_b32_e32 v22, v24
	v_permlane16_swap_b32_e32 v23, v25
	v_lshl_add_u64 v[248:249], v[20:21], 0, v[250:251]
	global_store_dwordx4 v[248:249], v[22:25], off
	s_nop 1
	v_pk_fma_f32 v[22:23], v[62:63], s[22:23], v[14:15] op_sel_hi:[1,0,1]
	v_pk_fma_f32 v[24:25], v[60:61], s[22:23], v[12:13] op_sel_hi:[1,0,1]
	v_pk_mul_f32 v[22:23], v[22:23], s[24:25] op_sel_hi:[1,0]
	v_pk_mul_f32 v[24:25], v[24:25], s[24:25] op_sel_hi:[1,0]
	v_pk_fma_f32 v[28:29], v[56:57], s[22:23], v[8:9] op_sel_hi:[1,0,1]
	v_med3_f32 v19, v24, s75, v210
	v_pk_mul_f32 v[28:29], v[28:29], s[24:25] op_sel_hi:[1,0]
	v_med3_f32 v24, v25, s75, v210
	v_med3_f32 v25, v22, s75, v210
	v_mov_b32_e32 v22, v165
	v_med3_f32 v30, v23, s75, v210
	v_cvt_pk_fp8_f32 v22, v19, v24
	v_med3_f32 v19, v28, s75, v210
	v_med3_f32 v24, v29, s75, v210
	v_mov_b32_e32 v23, v165
	v_cvt_pk_fp8_f32 v23, v19, v24
	v_pk_fma_f32 v[26:27], v[58:59], s[22:23], v[10:11] op_sel_hi:[1,0,1]
	v_cvt_pk_fp8_f32 v22, v25, v30 op_sel:[0,0,1]
	v_pk_mul_f32 v[26:27], v[26:27], s[24:25] op_sel_hi:[1,0]
	v_pk_fma_f32 v[30:31], v[48:49], s[22:23], v[0:1] op_sel_hi:[1,0,1]
	v_med3_f32 v19, v26, s75, v210
	v_med3_f32 v24, v27, s75, v210
	v_cvt_pk_fp8_f32 v23, v19, v24 op_sel:[0,0,1]
	v_pk_fma_f32 v[24:25], v[54:55], s[22:23], v[6:7] op_sel_hi:[1,0,1]
	v_pk_fma_f32 v[26:27], v[52:53], s[22:23], v[4:5] op_sel_hi:[1,0,1]
	v_pk_mul_f32 v[24:25], v[24:25], s[24:25] op_sel_hi:[1,0]
	v_pk_mul_f32 v[26:27], v[26:27], s[24:25] op_sel_hi:[1,0]
	v_pk_mul_f32 v[30:31], v[30:31], s[24:25] op_sel_hi:[1,0]
	v_med3_f32 v19, v26, s75, v210
	v_med3_f32 v26, v27, s75, v210
	v_med3_f32 v27, v24, s75, v210
	v_mov_b32_e32 v24, v165
	v_med3_f32 v48, v25, s75, v210
	v_cvt_pk_fp8_f32 v24, v19, v26
	v_med3_f32 v19, v30, s75, v210
	v_med3_f32 v26, v31, s75, v210
	v_mov_b32_e32 v25, v165
	v_cvt_pk_fp8_f32 v25, v19, v26
	v_pk_fma_f32 v[28:29], v[50:51], s[22:23], v[2:3] op_sel_hi:[1,0,1]
	v_add_u32_e32 v20, 0xa0, v18
	v_pk_mul_f32 v[28:29], v[28:29], s[24:25] op_sel_hi:[1,0]
	v_ashrrev_i32_e32 v21, 31, v20
	v_med3_f32 v19, v28, s75, v210
	v_med3_f32 v26, v29, s75, v210
	v_lshlrev_b64 v[20:21], 10, v[20:21]
	v_cvt_pk_fp8_f32 v24, v27, v48 op_sel:[0,0,1]
	v_cvt_pk_fp8_f32 v25, v19, v26 op_sel:[0,0,1]
	v_lshl_add_u64 v[20:21], s[12:13], 0, v[20:21]
	v_pk_fma_f32 v[12:13], v[44:45], s[22:23], v[12:13] op_sel_hi:[1,0,1]
	v_lshl_add_u64 v[20:21], v[20:21], 0, v[16:17]
	v_pk_mul_f32 v[12:13], v[12:13], s[24:25] op_sel_hi:[1,0]
	v_pk_fma_f32 v[8:9], v[40:41], s[22:23], v[8:9] op_sel_hi:[1,0,1]
	s_nop 1
	v_permlane16_swap_b32_e32 v22, v24
	v_permlane16_swap_b32_e32 v23, v25
	v_lshl_add_u64 v[248:249], v[20:21], 0, v[250:251]
	global_store_dwordx4 v[248:249], v[22:25], off
	s_nop 1
	v_pk_mul_f32 v[8:9], v[8:9], s[24:25] op_sel_hi:[1,0]
	v_med3_f32 v20, v12, s75, v210
	v_med3_f32 v13, v13, s75, v210
	v_mov_b32_e32 v12, v165
	v_cvt_pk_fp8_f32 v12, v20, v13
	v_med3_f32 v8, v8, s75, v210
	v_med3_f32 v9, v9, s75, v210
	v_mov_b32_e32 v13, v165
	v_cvt_pk_fp8_f32 v13, v8, v9
	v_pk_fma_f32 v[10:11], v[42:43], s[22:23], v[10:11] op_sel_hi:[1,0,1]
	v_pk_fma_f32 v[4:5], v[36:37], s[22:23], v[4:5] op_sel_hi:[1,0,1]
	v_pk_mul_f32 v[10:11], v[10:11], s[24:25] op_sel_hi:[1,0]
	v_pk_mul_f32 v[4:5], v[4:5], s[24:25] op_sel_hi:[1,0]
	v_med3_f32 v8, v10, s75, v210
	v_med3_f32 v9, v11, s75, v210
	v_pk_fma_f32 v[0:1], v[32:33], s[22:23], v[0:1] op_sel_hi:[1,0,1]
	v_cvt_pk_fp8_f32 v13, v8, v9 op_sel:[0,0,1]
	v_pk_mul_f32 v[0:1], v[0:1], s[24:25] op_sel_hi:[1,0]
	v_med3_f32 v8, v4, s75, v210
	v_med3_f32 v5, v5, s75, v210
	v_mov_b32_e32 v4, v165
	v_cvt_pk_fp8_f32 v4, v8, v5
	v_med3_f32 v0, v0, s75, v210
	v_med3_f32 v1, v1, s75, v210
	v_mov_b32_e32 v5, v165
	v_pk_fma_f32 v[14:15], v[46:47], s[22:23], v[14:15] op_sel_hi:[1,0,1]
	v_cvt_pk_fp8_f32 v5, v0, v1
	v_pk_mul_f32 v[14:15], v[14:15], s[24:25] op_sel_hi:[1,0]
	v_pk_fma_f32 v[6:7], v[38:39], s[22:23], v[6:7] op_sel_hi:[1,0,1]
	v_pk_fma_f32 v[2:3], v[34:35], s[22:23], v[2:3] op_sel_hi:[1,0,1]
	v_add_u32_e32 v18, 0xb0, v18
	v_med3_f32 v14, v14, s75, v210
	v_med3_f32 v15, v15, s75, v210
	v_pk_mul_f32 v[6:7], v[6:7], s[24:25] op_sel_hi:[1,0]
	v_pk_mul_f32 v[2:3], v[2:3], s[24:25] op_sel_hi:[1,0]
	v_ashrrev_i32_e32 v19, 31, v18
	v_cvt_pk_fp8_f32 v12, v14, v15 op_sel:[0,0,1]
	v_med3_f32 v6, v6, s75, v210
	v_med3_f32 v7, v7, s75, v210
	v_med3_f32 v0, v2, s75, v210
	v_med3_f32 v1, v3, s75, v210
	v_lshlrev_b64 v[18:19], 10, v[18:19]
	v_cvt_pk_fp8_f32 v4, v6, v7 op_sel:[0,0,1]
	v_cvt_pk_fp8_f32 v5, v0, v1 op_sel:[0,0,1]
	v_lshl_add_u64 v[0:1], s[12:13], 0, v[18:19]
	v_lshl_add_u64 v[0:1], v[0:1], 0, v[16:17]
	s_mov_b64 s[2:3], -1
	global_store_dwordx2 v[0:1], v[12:13], off
	global_store_dwordx2 v[0:1], v[4:5], off offset:128
	s_cbranch_vccnz .LBB0_664
	s_andn2_b64 vcc, exec, s[10:11]
	s_cbranch_vccnz .LBB0_663
	s_barrier
	s_branch .LBB0_663

.LBB0_822:
	v_mbcnt_lo_u32_b32 v250, -1, 0
	v_mbcnt_hi_u32_b32 v250, -1, v250
	v_bfe_u32 v250, v250, 4, 1
	v_mul_u32_u24_e32 v250, 0x78, v250
	v_mov_b32_e32 v251, 0
	s_lshl_b32 s26, s55, 8
	v_mov_b32_e32 v0, v199
	v_mov_b32_e32 v1, v198
	s_add_i32 s26, s26, s43
	v_pk_mul_f32 v[6:7], v[158:159], s[20:21] op_sel_hi:[1,0]
	v_add_u32_e32 v2, s26, v1
	v_ashrrev_i32_e32 v3, 31, v2
	v_pk_mul_f32 v[8:9], v[156:157], s[20:21] op_sel_hi:[1,0]
	v_lshlrev_b64 v[4:5], 12, v[2:3]
	v_pk_mul_f32 v[12:13], v[152:153], s[20:21] op_sel_hi:[1,0]
	v_med3_f32 v3, v8, s50, v210
	v_med3_f32 v8, v9, s50, v210
	v_med3_f32 v9, v6, s50, v210
	v_mov_b32_e32 v6, v165
	v_med3_f32 v14, v7, s50, v210
	v_cvt_pk_fp8_f32 v6, v3, v8
	v_med3_f32 v3, v12, s50, v210
	v_med3_f32 v8, v13, s50, v210
	v_mov_b32_e32 v7, v165
	v_cvt_pk_fp8_f32 v7, v3, v8
	v_pk_mul_f32 v[10:11], v[154:155], s[20:21] op_sel_hi:[1,0]
	v_cvt_pk_fp8_f32 v6, v9, v14 op_sel:[0,0,1]
	v_med3_f32 v3, v10, s50, v210
	v_med3_f32 v8, v11, s50, v210
	v_cvt_pk_fp8_f32 v7, v3, v8 op_sel:[0,0,1]
	v_pk_mul_f32 v[8:9], v[150:151], s[20:21] op_sel_hi:[1,0]
	v_pk_mul_f32 v[10:11], v[148:149], s[20:21] op_sel_hi:[1,0]
	v_pk_mul_f32 v[14:15], v[144:145], s[20:21] op_sel_hi:[1,0]
	v_med3_f32 v3, v10, s50, v210
	v_med3_f32 v10, v11, s50, v210
	v_med3_f32 v11, v8, s50, v210
	v_mov_b32_e32 v8, v165
	v_med3_f32 v16, v9, s50, v210
	v_cvt_pk_fp8_f32 v8, v3, v10
	v_med3_f32 v3, v14, s50, v210
	v_med3_f32 v10, v15, s50, v210
	v_mov_b32_e32 v9, v165
	v_cvt_pk_fp8_f32 v9, v3, v10
	s_lshl_b32 s26, s54, 8
	v_pk_mul_f32 v[12:13], v[146:147], s[20:21] op_sel_hi:[1,0]
	s_ashr_i32 s27, s26, 31
	v_lshl_add_u64 v[4:5], s[6:7], 0, v[4:5]
	v_med3_f32 v3, v12, s50, v210
	v_med3_f32 v10, v13, s50, v210
	v_lshlrev_b32_e32 v0, 3, v0
	v_lshl_add_u64 v[4:5], v[4:5], 0, s[26:27]
	v_cvt_pk_fp8_f32 v8, v11, v16 op_sel:[0,0,1]
	v_cvt_pk_fp8_f32 v9, v3, v10 op_sel:[0,0,1]
	v_ashrrev_i32_e32 v1, 31, v0
	v_lshl_add_u64 v[4:5], v[4:5], 0, s[16:17]
	v_lshl_add_u64 v[4:5], v[4:5], 0, v[0:1]
	s_nop 1
	v_permlane16_swap_b32_e32 v6, v8
	v_permlane16_swap_b32_e32 v7, v9
	v_lshl_add_u64 v[248:249], v[4:5], 0, v[250:251]
	global_store_dwordx4 v[248:249], v[6:9], off
	s_nop 1
	v_pk_mul_f32 v[6:7], v[142:143], s[20:21] op_sel_hi:[1,0]
	v_pk_mul_f32 v[8:9], v[140:141], s[20:21] op_sel_hi:[1,0]
	v_pk_mul_f32 v[12:13], v[136:137], s[20:21] op_sel_hi:[1,0]
	v_med3_f32 v3, v8, s50, v210
	v_med3_f32 v8, v9, s50, v210
	v_med3_f32 v9, v6, s50, v210
	v_mov_b32_e32 v6, v165
	v_med3_f32 v14, v7, s50, v210
	v_cvt_pk_fp8_f32 v6, v3, v8
	v_med3_f32 v3, v12, s50, v210
	v_med3_f32 v8, v13, s50, v210
	v_mov_b32_e32 v7, v165
	v_cvt_pk_fp8_f32 v7, v3, v8
	v_pk_mul_f32 v[10:11], v[138:139], s[20:21] op_sel_hi:[1,0]
	v_cvt_pk_fp8_f32 v6, v9, v14 op_sel:[0,0,1]
	v_med3_f32 v3, v10, s50, v210
	v_med3_f32 v8, v11, s50, v210
	v_cvt_pk_fp8_f32 v7, v3, v8 op_sel:[0,0,1]
	v_pk_mul_f32 v[8:9], v[134:135], s[20:21] op_sel_hi:[1,0]
	v_pk_mul_f32 v[10:11], v[132:133], s[20:21] op_sel_hi:[1,0]
	v_pk_mul_f32 v[14:15], v[128:129], s[20:21] op_sel_hi:[1,0]
	v_med3_f32 v3, v10, s50, v210
	v_med3_f32 v10, v11, s50, v210
	v_med3_f32 v11, v8, s50, v210
	v_mov_b32_e32 v8, v165
	v_med3_f32 v16, v9, s50, v210
	v_cvt_pk_fp8_f32 v8, v3, v10
	v_med3_f32 v3, v14, s50, v210
	v_med3_f32 v10, v15, s50, v210
	v_mov_b32_e32 v9, v165
	v_add_u32_e32 v4, 16, v2
	v_cvt_pk_fp8_f32 v9, v3, v10
	v_ashrrev_i32_e32 v5, 31, v4
	v_lshlrev_b64 v[4:5], 12, v[4:5]
	v_pk_mul_f32 v[12:13], v[130:131], s[20:21] op_sel_hi:[1,0]
	v_lshl_add_u64 v[4:5], s[6:7], 0, v[4:5]
	v_med3_f32 v3, v12, s50, v210
	v_med3_f32 v10, v13, s50, v210
	v_lshl_add_u64 v[4:5], v[4:5], 0, s[26:27]
	v_cvt_pk_fp8_f32 v8, v11, v16 op_sel:[0,0,1]
	v_cvt_pk_fp8_f32 v9, v3, v10 op_sel:[0,0,1]
	v_lshl_add_u64 v[4:5], v[4:5], 0, s[16:17]
	v_lshl_add_u64 v[4:5], v[4:5], 0, v[0:1]
	s_nop 1
	v_permlane16_swap_b32_e32 v6, v8
	v_permlane16_swap_b32_e32 v7, v9
	v_lshl_add_u64 v[248:249], v[4:5], 0, v[250:251]
	global_store_dwordx4 v[248:249], v[6:9], off
	s_nop 1
	v_pk_mul_f32 v[6:7], v[126:127], s[20:21] op_sel_hi:[1,0]
	v_pk_mul_f32 v[8:9], v[124:125], s[20:21] op_sel_hi:[1,0]
	v_pk_mul_f32 v[12:13], v[120:121], s[20:21] op_sel_hi:[1,0]
	v_med3_f32 v3, v8, s50, v210
	v_med3_f32 v8, v9, s50, v210
	v_med3_f32 v9, v6, s50, v210
	v_mov_b32_e32 v6, v165
	v_med3_f32 v14, v7, s50, v210
	v_cvt_pk_fp8_f32 v6, v3, v8
	v_med3_f32 v3, v12, s50, v210
	v_med3_f32 v8, v13, s50, v210
	v_mov_b32_e32 v7, v165
	v_cvt_pk_fp8_f32 v7, v3, v8
	v_pk_mul_f32 v[10:11], v[122:123], s[20:21] op_sel_hi:[1,0]
	v_cvt_pk_fp8_f32 v6, v9, v14 op_sel:[0,0,1]
	v_med3_f32 v3, v10, s50, v210
	v_med3_f32 v8, v11, s50, v210
	v_cvt_pk_fp8_f32 v7, v3, v8 op_sel:[0,0,1]
	v_pk_mul_f32 v[8:9], v[118:119], s[20:21] op_sel_hi:[1,0]
	v_pk_mul_f32 v[10:11], v[116:117], s[20:21] op_sel_hi:[1,0]
	v_pk_mul_f32 v[14:15], v[112:113], s[20:21] op_sel_hi:[1,0]
	v_med3_f32 v3, v10, s50, v210
	v_med3_f32 v10, v11, s50, v210
	v_med3_f32 v11, v8, s50, v210
	v_mov_b32_e32 v8, v165
	v_med3_f32 v16, v9, s50, v210
	v_cvt_pk_fp8_f32 v8, v3, v10
	v_med3_f32 v3, v14, s50, v210
	v_med3_f32 v10, v15, s50, v210
	v_mov_b32_e32 v9, v165
	v_add_u32_e32 v4, 32, v2
	v_cvt_pk_fp8_f32 v9, v3, v10
	v_ashrrev_i32_e32 v5, 31, v4
	v_lshlrev_b64 v[4:5], 12, v[4:5]
	v_pk_mul_f32 v[12:13], v[114:115], s[20:21] op_sel_hi:[1,0]
	v_lshl_add_u64 v[4:5], s[6:7], 0, v[4:5]
	v_med3_f32 v3, v12, s50, v210
	v_med3_f32 v10, v13, s50, v210
	v_lshl_add_u64 v[4:5], v[4:5], 0, s[26:27]
	v_cvt_pk_fp8_f32 v8, v11, v16 op_sel:[0,0,1]
	v_cvt_pk_fp8_f32 v9, v3, v10 op_sel:[0,0,1]
	v_lshl_add_u64 v[4:5], v[4:5], 0, s[16:17]
	v_lshl_add_u64 v[4:5], v[4:5], 0, v[0:1]
	s_nop 1
	v_permlane16_swap_b32_e32 v6, v8
	v_permlane16_swap_b32_e32 v7, v9
	v_lshl_add_u64 v[248:249], v[4:5], 0, v[250:251]
	global_store_dwordx4 v[248:249], v[6:9], off
	s_nop 1
	v_pk_mul_f32 v[6:7], v[110:111], s[20:21] op_sel_hi:[1,0]
	v_pk_mul_f32 v[8:9], v[108:109], s[20:21] op_sel_hi:[1,0]
	v_pk_mul_f32 v[12:13], v[104:105], s[20:21] op_sel_hi:[1,0]
	v_med3_f32 v3, v8, s50, v210
	v_med3_f32 v8, v9, s50, v210
	v_med3_f32 v9, v6, s50, v210
	v_mov_b32_e32 v6, v165
	v_med3_f32 v14, v7, s50, v210
	v_cvt_pk_fp8_f32 v6, v3, v8
	v_med3_f32 v3, v12, s50, v210
	v_med3_f32 v8, v13, s50, v210
	v_mov_b32_e32 v7, v165
	v_cvt_pk_fp8_f32 v7, v3, v8
	v_pk_mul_f32 v[10:11], v[106:107], s[20:21] op_sel_hi:[1,0]
	v_cvt_pk_fp8_f32 v6, v9, v14 op_sel:[0,0,1]
	v_med3_f32 v3, v10, s50, v210
	v_med3_f32 v8, v11, s50, v210
	v_cvt_pk_fp8_f32 v7, v3, v8 op_sel:[0,0,1]
	v_pk_mul_f32 v[8:9], v[102:103], s[20:21] op_sel_hi:[1,0]
	v_pk_mul_f32 v[10:11], v[100:101], s[20:21] op_sel_hi:[1,0]
	v_pk_mul_f32 v[14:15], v[96:97], s[20:21] op_sel_hi:[1,0]
	v_med3_f32 v3, v10, s50, v210
	v_med3_f32 v10, v11, s50, v210
	v_med3_f32 v11, v8, s50, v210
	v_mov_b32_e32 v8, v165
	v_med3_f32 v16, v9, s50, v210
	v_cvt_pk_fp8_f32 v8, v3, v10
	v_med3_f32 v3, v14, s50, v210
	v_med3_f32 v10, v15, s50, v210
	v_mov_b32_e32 v9, v165
	v_add_u32_e32 v4, 48, v2
	v_cvt_pk_fp8_f32 v9, v3, v10
	v_ashrrev_i32_e32 v5, 31, v4
	v_lshlrev_b64 v[4:5], 12, v[4:5]
	v_pk_mul_f32 v[12:13], v[98:99], s[20:21] op_sel_hi:[1,0]
	v_lshl_add_u64 v[4:5], s[6:7], 0, v[4:5]
	v_med3_f32 v3, v12, s50, v210
	v_med3_f32 v10, v13, s50, v210
	v_lshl_add_u64 v[4:5], v[4:5], 0, s[26:27]
	v_cvt_pk_fp8_f32 v8, v11, v16 op_sel:[0,0,1]
	v_cvt_pk_fp8_f32 v9, v3, v10 op_sel:[0,0,1]
	v_lshl_add_u64 v[4:5], v[4:5], 0, s[16:17]
	v_lshl_add_u64 v[4:5], v[4:5], 0, v[0:1]
	s_nop 1
	v_permlane16_swap_b32_e32 v6, v8
	v_permlane16_swap_b32_e32 v7, v9
	v_lshl_add_u64 v[248:249], v[4:5], 0, v[250:251]
	global_store_dwordx4 v[248:249], v[6:9], off
	s_nop 1
	v_pk_mul_f32 v[6:7], v[94:95], s[20:21] op_sel_hi:[1,0]
	v_pk_mul_f32 v[8:9], v[92:93], s[20:21] op_sel_hi:[1,0]
	v_pk_mul_f32 v[12:13], v[88:89], s[20:21] op_sel_hi:[1,0]
	v_med3_f32 v3, v8, s50, v210
	v_med3_f32 v8, v9, s50, v210
	v_med3_f32 v9, v6, s50, v210
	v_mov_b32_e32 v6, v165
	v_med3_f32 v14, v7, s50, v210
	v_cvt_pk_fp8_f32 v6, v3, v8
	v_med3_f32 v3, v12, s50, v210
	v_med3_f32 v8, v13, s50, v210
	v_mov_b32_e32 v7, v165
	v_cvt_pk_fp8_f32 v7, v3, v8
	v_pk_mul_f32 v[10:11], v[90:91], s[20:21] op_sel_hi:[1,0]
	v_cvt_pk_fp8_f32 v6, v9, v14 op_sel:[0,0,1]
	v_med3_f32 v3, v10, s50, v210
	v_med3_f32 v8, v11, s50, v210
	v_cvt_pk_fp8_f32 v7, v3, v8 op_sel:[0,0,1]
	v_pk_mul_f32 v[8:9], v[86:87], s[20:21] op_sel_hi:[1,0]
	v_pk_mul_f32 v[10:11], v[84:85], s[20:21] op_sel_hi:[1,0]
	v_pk_mul_f32 v[14:15], v[80:81], s[20:21] op_sel_hi:[1,0]
	v_med3_f32 v3, v10, s50, v210
	v_med3_f32 v10, v11, s50, v210
	v_med3_f32 v11, v8, s50, v210
	v_mov_b32_e32 v8, v165
	v_med3_f32 v16, v9, s50, v210
	v_cvt_pk_fp8_f32 v8, v3, v10
	v_med3_f32 v3, v14, s50, v210
	v_med3_f32 v10, v15, s50, v210
	v_mov_b32_e32 v9, v165
	v_add_u32_e32 v4, 0x80, v2
	v_cvt_pk_fp8_f32 v9, v3, v10
	v_ashrrev_i32_e32 v5, 31, v4
	v_lshlrev_b64 v[4:5], 12, v[4:5]
	v_pk_mul_f32 v[12:13], v[82:83], s[20:21] op_sel_hi:[1,0]
	v_lshl_add_u64 v[4:5], s[6:7], 0, v[4:5]
	v_med3_f32 v3, v12, s50, v210
	v_med3_f32 v10, v13, s50, v210
	v_lshl_add_u64 v[4:5], v[4:5], 0, s[26:27]
	v_cvt_pk_fp8_f32 v8, v11, v16 op_sel:[0,0,1]
	v_cvt_pk_fp8_f32 v9, v3, v10 op_sel:[0,0,1]
	v_lshl_add_u64 v[4:5], v[4:5], 0, s[16:17]
	v_lshl_add_u64 v[4:5], v[4:5], 0, v[0:1]
	s_nop 1
	v_permlane16_swap_b32_e32 v6, v8
	v_permlane16_swap_b32_e32 v7, v9
	v_lshl_add_u64 v[248:249], v[4:5], 0, v[250:251]
	global_store_dwordx4 v[248:249], v[6:9], off
	s_nop 1
	v_pk_mul_f32 v[6:7], v[78:79], s[20:21] op_sel_hi:[1,0]
	v_pk_mul_f32 v[8:9], v[76:77], s[20:21] op_sel_hi:[1,0]
	v_pk_mul_f32 v[12:13], v[72:73], s[20:21] op_sel_hi:[1,0]
	v_med3_f32 v3, v8, s50, v210
	v_med3_f32 v8, v9, s50, v210
	v_med3_f32 v9, v6, s50, v210
	v_mov_b32_e32 v6, v165
	v_med3_f32 v14, v7, s50, v210
	v_cvt_pk_fp8_f32 v6, v3, v8
	v_med3_f32 v3, v12, s50, v210
	v_med3_f32 v8, v13, s50, v210
	v_mov_b32_e32 v7, v165
	v_cvt_pk_fp8_f32 v7, v3, v8
	v_pk_mul_f32 v[10:11], v[74:75], s[20:21] op_sel_hi:[1,0]
	v_cvt_pk_fp8_f32 v6, v9, v14 op_sel:[0,0,1]
	v_med3_f32 v3, v10, s50, v210
	v_med3_f32 v8, v11, s50, v210
	v_cvt_pk_fp8_f32 v7, v3, v8 op_sel:[0,0,1]
	v_pk_mul_f32 v[8:9], v[70:71], s[20:21] op_sel_hi:[1,0]
	v_pk_mul_f32 v[10:11], v[68:69], s[20:21] op_sel_hi:[1,0]
	v_pk_mul_f32 v[14:15], v[64:65], s[20:21] op_sel_hi:[1,0]
	v_med3_f32 v3, v10, s50, v210
	v_med3_f32 v10, v11, s50, v210
	v_med3_f32 v11, v8, s50, v210
	v_mov_b32_e32 v8, v165
	v_med3_f32 v16, v9, s50, v210
	v_cvt_pk_fp8_f32 v8, v3, v10
	v_med3_f32 v3, v14, s50, v210
	v_med3_f32 v10, v15, s50, v210
	v_mov_b32_e32 v9, v165
	v_add_u32_e32 v4, 0x90, v2
	v_cvt_pk_fp8_f32 v9, v3, v10
	v_ashrrev_i32_e32 v5, 31, v4
	v_lshlrev_b64 v[4:5], 12, v[4:5]
	v_pk_mul_f32 v[12:13], v[66:67], s[20:21] op_sel_hi:[1,0]
	v_lshl_add_u64 v[4:5], s[6:7], 0, v[4:5]
	v_med3_f32 v3, v12, s50, v210
	v_med3_f32 v10, v13, s50, v210
	v_lshl_add_u64 v[4:5], v[4:5], 0, s[26:27]
	v_cvt_pk_fp8_f32 v8, v11, v16 op_sel:[0,0,1]
	v_cvt_pk_fp8_f32 v9, v3, v10 op_sel:[0,0,1]
	v_lshl_add_u64 v[4:5], v[4:5], 0, s[16:17]
	v_lshl_add_u64 v[4:5], v[4:5], 0, v[0:1]
	s_nop 1
	v_permlane16_swap_b32_e32 v6, v8
	v_permlane16_swap_b32_e32 v7, v9
	v_lshl_add_u64 v[248:249], v[4:5], 0, v[250:251]
	global_store_dwordx4 v[248:249], v[6:9], off
	s_nop 1
	v_pk_mul_f32 v[6:7], v[62:63], s[20:21] op_sel_hi:[1,0]
	v_pk_mul_f32 v[8:9], v[60:61], s[20:21] op_sel_hi:[1,0]
	v_pk_mul_f32 v[12:13], v[56:57], s[20:21] op_sel_hi:[1,0]
	v_med3_f32 v3, v8, s50, v210
	v_med3_f32 v8, v9, s50, v210
	v_med3_f32 v9, v6, s50, v210
	v_mov_b32_e32 v6, v165
	v_med3_f32 v14, v7, s50, v210
	v_cvt_pk_fp8_f32 v6, v3, v8
	v_med3_f32 v3, v12, s50, v210
	v_med3_f32 v8, v13, s50, v210
	v_mov_b32_e32 v7, v165
	v_cvt_pk_fp8_f32 v7, v3, v8
	v_pk_mul_f32 v[10:11], v[58:59], s[20:21] op_sel_hi:[1,0]
	v_cvt_pk_fp8_f32 v6, v9, v14 op_sel:[0,0,1]
	v_med3_f32 v3, v10, s50, v210
	v_med3_f32 v8, v11, s50, v210
	v_cvt_pk_fp8_f32 v7, v3, v8 op_sel:[0,0,1]
	v_pk_mul_f32 v[8:9], v[54:55], s[20:21] op_sel_hi:[1,0]
	v_pk_mul_f32 v[10:11], v[52:53], s[20:21] op_sel_hi:[1,0]
	v_pk_mul_f32 v[14:15], v[48:49], s[20:21] op_sel_hi:[1,0]
	v_med3_f32 v3, v10, s50, v210
	v_med3_f32 v10, v11, s50, v210
	v_med3_f32 v11, v8, s50, v210
	v_mov_b32_e32 v8, v165
	v_med3_f32 v16, v9, s50, v210
	v_cvt_pk_fp8_f32 v8, v3, v10
	v_med3_f32 v3, v14, s50, v210
	v_med3_f32 v10, v15, s50, v210
	v_mov_b32_e32 v9, v165
	v_add_u32_e32 v4, 0xa0, v2
	v_cvt_pk_fp8_f32 v9, v3, v10
	v_ashrrev_i32_e32 v5, 31, v4
	v_lshlrev_b64 v[4:5], 12, v[4:5]
	v_pk_mul_f32 v[12:13], v[50:51], s[20:21] op_sel_hi:[1,0]
	v_lshl_add_u64 v[4:5], s[6:7], 0, v[4:5]
	v_med3_f32 v3, v12, s50, v210
	v_med3_f32 v10, v13, s50, v210
	v_lshl_add_u64 v[4:5], v[4:5], 0, s[26:27]
	v_cvt_pk_fp8_f32 v8, v11, v16 op_sel:[0,0,1]
	v_cvt_pk_fp8_f32 v9, v3, v10 op_sel:[0,0,1]
	v_lshl_add_u64 v[4:5], v[4:5], 0, s[16:17]
	v_lshl_add_u64 v[4:5], v[4:5], 0, v[0:1]
	s_nop 1
	v_permlane16_swap_b32_e32 v6, v8
	v_permlane16_swap_b32_e32 v7, v9
	v_lshl_add_u64 v[248:249], v[4:5], 0, v[250:251]
	global_store_dwordx4 v[248:249], v[6:9], off
	s_nop 1
	v_pk_mul_f32 v[4:5], v[46:47], s[20:21] op_sel_hi:[1,0]
	v_pk_mul_f32 v[6:7], v[44:45], s[20:21] op_sel_hi:[1,0]
	v_pk_mul_f32 v[10:11], v[40:41], s[20:21] op_sel_hi:[1,0]
	v_med3_f32 v6, v6, s50, v210
	v_med3_f32 v7, v7, s50, v210
	v_med3_f32 v12, v4, s50, v210
	v_mov_b32_e32 v4, v165
	v_med3_f32 v13, v5, s50, v210
	v_cvt_pk_fp8_f32 v4, v6, v7
	v_med3_f32 v6, v10, s50, v210
	v_med3_f32 v7, v11, s50, v210
	v_mov_b32_e32 v5, v165
	v_cvt_pk_fp8_f32 v5, v6, v7
	v_pk_mul_f32 v[8:9], v[42:43], s[20:21] op_sel_hi:[1,0]
	v_cvt_pk_fp8_f32 v4, v12, v13 op_sel:[0,0,1]
	v_med3_f32 v6, v8, s50, v210
	v_med3_f32 v7, v9, s50, v210
	v_cvt_pk_fp8_f32 v5, v6, v7 op_sel:[0,0,1]
	v_pk_mul_f32 v[6:7], v[38:39], s[20:21] op_sel_hi:[1,0]
	v_pk_mul_f32 v[8:9], v[36:37], s[20:21] op_sel_hi:[1,0]
	v_pk_mul_f32 v[12:13], v[32:33], s[20:21] op_sel_hi:[1,0]
	v_med3_f32 v8, v8, s50, v210
	v_med3_f32 v9, v9, s50, v210
	v_med3_f32 v14, v6, s50, v210
	v_mov_b32_e32 v6, v165
	v_med3_f32 v15, v7, s50, v210
	v_cvt_pk_fp8_f32 v6, v8, v9
	v_med3_f32 v8, v12, s50, v210
	v_med3_f32 v9, v13, s50, v210
	v_mov_b32_e32 v7, v165
	v_add_u32_e32 v2, 0xb0, v2
	v_cvt_pk_fp8_f32 v7, v8, v9
	v_ashrrev_i32_e32 v3, 31, v2
	v_lshlrev_b64 v[2:3], 12, v[2:3]
	v_pk_mul_f32 v[10:11], v[34:35], s[20:21] op_sel_hi:[1,0]
	v_lshl_add_u64 v[2:3], s[6:7], 0, v[2:3]
	v_med3_f32 v8, v10, s50, v210
	v_med3_f32 v9, v11, s50, v210
	v_lshl_add_u64 v[2:3], v[2:3], 0, s[26:27]
	v_cvt_pk_fp8_f32 v6, v14, v15 op_sel:[0,0,1]
	v_cvt_pk_fp8_f32 v7, v8, v9 op_sel:[0,0,1]
	v_lshl_add_u64 v[2:3], v[2:3], 0, s[16:17]
	v_lshl_add_u64 v[0:1], v[2:3], 0, v[0:1]
	s_and_b64 vcc, exec, s[2:3]
	s_mov_b64 s[2:3], -1
	s_nop 1
	v_permlane16_swap_b32_e32 v4, v6
	v_permlane16_swap_b32_e32 v5, v7
	v_lshl_add_u64 v[248:249], v[0:1], 0, v[250:251]
	global_store_dwordx4 v[248:249], v[4:7], off
	s_nop 1
	s_cbranch_vccnz .LBB0_811
	s_andn2_b64 vcc, exec, s[4:5]
	s_cbranch_vccnz .LBB0_810
	s_barrier
	s_branch .LBB0_810

.LBB0_1794:
	v_mbcnt_lo_u32_b32 v250, -1, 0
	v_mbcnt_hi_u32_b32 v250, -1, v250
	v_bfe_u32 v250, v250, 4, 1
	v_mul_u32_u24_e32 v250, 0x78, v250
	v_mov_b32_e32 v251, 0
	s_and_b64 vcc, exec, s[20:21]
	s_cbranch_vccz .LBB0_1796
	s_barrier
.LBB0_1796:
	s_lshl_b32 s27, s81, 10
	s_and_b32 s27, s27, 0x400
	v_mov_b32_e32 v17, v171
	v_mov_b32_e32 v16, v204
	s_add_i32 s27, s67, s27
	s_and_b64 vcc, exec, s[2:3]
	v_lshl_add_u32 v0, v16, 5, s27
	s_lshl_b32 s27, s80, 8
	s_or_b32 s27, s27, s66
	ds_read_b128 v[12:15], v0
	ds_read_b128 v[8:11], v0 offset:16
	ds_read_b128 v[4:7], v0 offset:512
	ds_read_b128 v[0:3], v0 offset:528
	v_lshl_add_u32 v16, v16, 3, s27
	s_lshl_b32 s27, s79, 8
	s_add_i32 s27, s27, s68
	v_add_u32_e32 v18, s27, v17
	s_waitcnt lgkmcnt(0)
	v_pk_fma_f32 v[22:23], v[158:159], s[22:23], v[14:15] op_sel_hi:[1,0,1]
	v_pk_fma_f32 v[24:25], v[156:157], s[22:23], v[12:13] op_sel_hi:[1,0,1]
	v_ashrrev_i32_e32 v19, 31, v18
	v_pk_mul_f32 v[22:23], v[22:23], s[24:25] op_sel_hi:[1,0]
	v_pk_mul_f32 v[24:25], v[24:25], s[24:25] op_sel_hi:[1,0]
	v_pk_fma_f32 v[28:29], v[152:153], s[22:23], v[8:9] op_sel_hi:[1,0,1]
	v_lshlrev_b64 v[20:21], 10, v[18:19]
	v_pk_mul_f32 v[28:29], v[28:29], s[24:25] op_sel_hi:[1,0]
	v_med3_f32 v19, v24, s75, v210
	v_med3_f32 v24, v25, s75, v210
	v_med3_f32 v25, v22, s75, v210
	v_mov_b32_e32 v22, v165
	v_med3_f32 v30, v23, s75, v210
	v_cvt_pk_fp8_f32 v22, v19, v24
	v_med3_f32 v19, v28, s75, v210
	v_med3_f32 v24, v29, s75, v210
	v_mov_b32_e32 v23, v165
	v_cvt_pk_fp8_f32 v23, v19, v24
	v_pk_fma_f32 v[26:27], v[154:155], s[22:23], v[10:11] op_sel_hi:[1,0,1]
	v_cvt_pk_fp8_f32 v22, v25, v30 op_sel:[0,0,1]
	v_pk_mul_f32 v[26:27], v[26:27], s[24:25] op_sel_hi:[1,0]
	v_pk_fma_f32 v[30:31], v[144:145], s[22:23], v[0:1] op_sel_hi:[1,0,1]
	v_med3_f32 v19, v26, s75, v210
	v_med3_f32 v24, v27, s75, v210
	v_cvt_pk_fp8_f32 v23, v19, v24 op_sel:[0,0,1]
	v_pk_fma_f32 v[24:25], v[150:151], s[22:23], v[6:7] op_sel_hi:[1,0,1]
	v_pk_fma_f32 v[26:27], v[148:149], s[22:23], v[4:5] op_sel_hi:[1,0,1]
	v_pk_mul_f32 v[24:25], v[24:25], s[24:25] op_sel_hi:[1,0]
	v_pk_mul_f32 v[26:27], v[26:27], s[24:25] op_sel_hi:[1,0]
	v_pk_mul_f32 v[30:31], v[30:31], s[24:25] op_sel_hi:[1,0]
	v_med3_f32 v19, v26, s75, v210
	v_med3_f32 v26, v27, s75, v210
	v_med3_f32 v27, v24, s75, v210
	v_mov_b32_e32 v24, v165
	v_med3_f32 v144, v25, s75, v210
	v_cvt_pk_fp8_f32 v24, v19, v26
	v_med3_f32 v19, v30, s75, v210
	v_med3_f32 v26, v31, s75, v210
	v_mov_b32_e32 v25, v165
	v_cvt_pk_fp8_f32 v25, v19, v26
	v_pk_fma_f32 v[28:29], v[146:147], s[22:23], v[2:3] op_sel_hi:[1,0,1]
	v_cvt_pk_fp8_f32 v24, v27, v144 op_sel:[0,0,1]
	v_pk_mul_f32 v[28:29], v[28:29], s[24:25] op_sel_hi:[1,0]
	v_ashrrev_i32_e32 v17, 31, v16
	v_med3_f32 v19, v28, s75, v210
	v_med3_f32 v26, v29, s75, v210
	v_cvt_pk_fp8_f32 v25, v19, v26 op_sel:[0,0,1]
	v_lshl_add_u64 v[20:21], s[12:13], 0, v[20:21]
	v_lshl_add_u64 v[20:21], v[20:21], 0, v[16:17]
	s_nop 1
	v_permlane16_swap_b32_e32 v22, v24
	v_permlane16_swap_b32_e32 v23, v25
	v_lshl_add_u64 v[248:249], v[20:21], 0, v[250:251]
	global_store_dwordx4 v[248:249], v[22:25], off
	s_nop 1
	v_pk_fma_f32 v[22:23], v[142:143], s[22:23], v[14:15] op_sel_hi:[1,0,1]
	v_pk_fma_f32 v[24:25], v[140:141], s[22:23], v[12:13] op_sel_hi:[1,0,1]
	v_pk_mul_f32 v[22:23], v[22:23], s[24:25] op_sel_hi:[1,0]
	v_pk_mul_f32 v[24:25], v[24:25], s[24:25] op_sel_hi:[1,0]
	v_pk_fma_f32 v[28:29], v[136:137], s[22:23], v[8:9] op_sel_hi:[1,0,1]
	v_med3_f32 v19, v24, s75, v210
	v_pk_mul_f32 v[28:29], v[28:29], s[24:25] op_sel_hi:[1,0]
	v_med3_f32 v24, v25, s75, v210
	v_med3_f32 v25, v22, s75, v210
	v_mov_b32_e32 v22, v165
	v_med3_f32 v30, v23, s75, v210
	v_cvt_pk_fp8_f32 v22, v19, v24
	v_med3_f32 v19, v28, s75, v210
	v_med3_f32 v24, v29, s75, v210
	v_mov_b32_e32 v23, v165
	v_cvt_pk_fp8_f32 v23, v19, v24
	v_pk_fma_f32 v[26:27], v[138:139], s[22:23], v[10:11] op_sel_hi:[1,0,1]
	v_cvt_pk_fp8_f32 v22, v25, v30 op_sel:[0,0,1]
	v_pk_mul_f32 v[26:27], v[26:27], s[24:25] op_sel_hi:[1,0]
	v_pk_fma_f32 v[30:31], v[128:129], s[22:23], v[0:1] op_sel_hi:[1,0,1]
	v_med3_f32 v19, v26, s75, v210
	v_med3_f32 v24, v27, s75, v210
	v_cvt_pk_fp8_f32 v23, v19, v24 op_sel:[0,0,1]
	v_pk_fma_f32 v[24:25], v[134:135], s[22:23], v[6:7] op_sel_hi:[1,0,1]
	v_pk_fma_f32 v[26:27], v[132:133], s[22:23], v[4:5] op_sel_hi:[1,0,1]
	v_pk_mul_f32 v[24:25], v[24:25], s[24:25] op_sel_hi:[1,0]
	v_pk_mul_f32 v[26:27], v[26:27], s[24:25] op_sel_hi:[1,0]
	v_pk_mul_f32 v[30:31], v[30:31], s[24:25] op_sel_hi:[1,0]
	v_med3_f32 v19, v26, s75, v210
	v_med3_f32 v26, v27, s75, v210
	v_med3_f32 v27, v24, s75, v210
	v_mov_b32_e32 v24, v165
	v_med3_f32 v128, v25, s75, v210
	v_cvt_pk_fp8_f32 v24, v19, v26
	v_med3_f32 v19, v30, s75, v210
	v_med3_f32 v26, v31, s75, v210
	v_mov_b32_e32 v25, v165
	v_cvt_pk_fp8_f32 v25, v19, v26
	v_pk_fma_f32 v[28:29], v[130:131], s[22:23], v[2:3] op_sel_hi:[1,0,1]
	v_add_u32_e32 v20, 16, v18
	v_pk_mul_f32 v[28:29], v[28:29], s[24:25] op_sel_hi:[1,0]
	v_ashrrev_i32_e32 v21, 31, v20
	v_med3_f32 v19, v28, s75, v210
	v_med3_f32 v26, v29, s75, v210
	v_lshlrev_b64 v[20:21], 10, v[20:21]
	v_cvt_pk_fp8_f32 v24, v27, v128 op_sel:[0,0,1]
	v_cvt_pk_fp8_f32 v25, v19, v26 op_sel:[0,0,1]
	v_lshl_add_u64 v[20:21], s[12:13], 0, v[20:21]
	v_lshl_add_u64 v[20:21], v[20:21], 0, v[16:17]
	s_nop 1
	v_permlane16_swap_b32_e32 v22, v24
	v_permlane16_swap_b32_e32 v23, v25
	v_lshl_add_u64 v[248:249], v[20:21], 0, v[250:251]
	global_store_dwordx4 v[248:249], v[22:25], off
	s_nop 1
	v_pk_fma_f32 v[22:23], v[126:127], s[22:23], v[14:15] op_sel_hi:[1,0,1]
	v_pk_fma_f32 v[24:25], v[124:125], s[22:23], v[12:13] op_sel_hi:[1,0,1]
	v_pk_mul_f32 v[22:23], v[22:23], s[24:25] op_sel_hi:[1,0]
	v_pk_mul_f32 v[24:25], v[24:25], s[24:25] op_sel_hi:[1,0]
	v_pk_fma_f32 v[28:29], v[120:121], s[22:23], v[8:9] op_sel_hi:[1,0,1]
	v_med3_f32 v19, v24, s75, v210
	v_pk_mul_f32 v[28:29], v[28:29], s[24:25] op_sel_hi:[1,0]
	v_med3_f32 v24, v25, s75, v210
	v_med3_f32 v25, v22, s75, v210
	v_mov_b32_e32 v22, v165
	v_med3_f32 v30, v23, s75, v210
	v_cvt_pk_fp8_f32 v22, v19, v24
	v_med3_f32 v19, v28, s75, v210
	v_med3_f32 v24, v29, s75, v210
	v_mov_b32_e32 v23, v165
	v_cvt_pk_fp8_f32 v23, v19, v24
	v_pk_fma_f32 v[26:27], v[122:123], s[22:23], v[10:11] op_sel_hi:[1,0,1]
	v_cvt_pk_fp8_f32 v22, v25, v30 op_sel:[0,0,1]
	v_pk_mul_f32 v[26:27], v[26:27], s[24:25] op_sel_hi:[1,0]
	v_pk_fma_f32 v[30:31], v[112:113], s[22:23], v[0:1] op_sel_hi:[1,0,1]
	v_med3_f32 v19, v26, s75, v210
	v_med3_f32 v24, v27, s75, v210
	v_cvt_pk_fp8_f32 v23, v19, v24 op_sel:[0,0,1]
	v_pk_fma_f32 v[24:25], v[118:119], s[22:23], v[6:7] op_sel_hi:[1,0,1]
	v_pk_fma_f32 v[26:27], v[116:117], s[22:23], v[4:5] op_sel_hi:[1,0,1]
	v_pk_mul_f32 v[24:25], v[24:25], s[24:25] op_sel_hi:[1,0]
	v_pk_mul_f32 v[26:27], v[26:27], s[24:25] op_sel_hi:[1,0]
	v_pk_mul_f32 v[30:31], v[30:31], s[24:25] op_sel_hi:[1,0]
	v_med3_f32 v19, v26, s75, v210
	v_med3_f32 v26, v27, s75, v210
	v_med3_f32 v27, v24, s75, v210
	v_mov_b32_e32 v24, v165
	v_med3_f32 v112, v25, s75, v210
	v_cvt_pk_fp8_f32 v24, v19, v26
	v_med3_f32 v19, v30, s75, v210
	v_med3_f32 v26, v31, s75, v210
	v_mov_b32_e32 v25, v165
	v_cvt_pk_fp8_f32 v25, v19, v26
	v_pk_fma_f32 v[28:29], v[114:115], s[22:23], v[2:3] op_sel_hi:[1,0,1]
	v_add_u32_e32 v20, 32, v18
	v_pk_mul_f32 v[28:29], v[28:29], s[24:25] op_sel_hi:[1,0]
	v_ashrrev_i32_e32 v21, 31, v20
	v_med3_f32 v19, v28, s75, v210
	v_med3_f32 v26, v29, s75, v210
	v_lshlrev_b64 v[20:21], 10, v[20:21]
	v_cvt_pk_fp8_f32 v24, v27, v112 op_sel:[0,0,1]
	v_cvt_pk_fp8_f32 v25, v19, v26 op_sel:[0,0,1]
	v_lshl_add_u64 v[20:21], s[12:13], 0, v[20:21]
	v_lshl_add_u64 v[20:21], v[20:21], 0, v[16:17]
	s_nop 1
	v_permlane16_swap_b32_e32 v22, v24
	v_permlane16_swap_b32_e32 v23, v25
	v_lshl_add_u64 v[248:249], v[20:21], 0, v[250:251]
	global_store_dwordx4 v[248:249], v[22:25], off
	s_nop 1
	v_pk_fma_f32 v[22:23], v[110:111], s[22:23], v[14:15] op_sel_hi:[1,0,1]
	v_pk_fma_f32 v[24:25], v[108:109], s[22:23], v[12:13] op_sel_hi:[1,0,1]
	v_pk_mul_f32 v[22:23], v[22:23], s[24:25] op_sel_hi:[1,0]
	v_pk_mul_f32 v[24:25], v[24:25], s[24:25] op_sel_hi:[1,0]
	v_pk_fma_f32 v[28:29], v[104:105], s[22:23], v[8:9] op_sel_hi:[1,0,1]
	v_med3_f32 v19, v24, s75, v210
	v_pk_mul_f32 v[28:29], v[28:29], s[24:25] op_sel_hi:[1,0]
	v_med3_f32 v24, v25, s75, v210
	v_med3_f32 v25, v22, s75, v210
	v_mov_b32_e32 v22, v165
	v_med3_f32 v30, v23, s75, v210
	v_cvt_pk_fp8_f32 v22, v19, v24
	v_med3_f32 v19, v28, s75, v210
	v_med3_f32 v24, v29, s75, v210
	v_mov_b32_e32 v23, v165
	v_cvt_pk_fp8_f32 v23, v19, v24
	v_pk_fma_f32 v[26:27], v[106:107], s[22:23], v[10:11] op_sel_hi:[1,0,1]
	v_cvt_pk_fp8_f32 v22, v25, v30 op_sel:[0,0,1]
	v_pk_mul_f32 v[26:27], v[26:27], s[24:25] op_sel_hi:[1,0]
	v_pk_fma_f32 v[30:31], v[96:97], s[22:23], v[0:1] op_sel_hi:[1,0,1]
	v_med3_f32 v19, v26, s75, v210
	v_med3_f32 v24, v27, s75, v210
	v_cvt_pk_fp8_f32 v23, v19, v24 op_sel:[0,0,1]
	v_pk_fma_f32 v[24:25], v[102:103], s[22:23], v[6:7] op_sel_hi:[1,0,1]
	v_pk_fma_f32 v[26:27], v[100:101], s[22:23], v[4:5] op_sel_hi:[1,0,1]
	v_pk_mul_f32 v[24:25], v[24:25], s[24:25] op_sel_hi:[1,0]
	v_pk_mul_f32 v[26:27], v[26:27], s[24:25] op_sel_hi:[1,0]
	v_pk_mul_f32 v[30:31], v[30:31], s[24:25] op_sel_hi:[1,0]
	v_med3_f32 v19, v26, s75, v210
	v_med3_f32 v26, v27, s75, v210
	v_med3_f32 v27, v24, s75, v210
	v_mov_b32_e32 v24, v165
	v_med3_f32 v96, v25, s75, v210
	v_cvt_pk_fp8_f32 v24, v19, v26
	v_med3_f32 v19, v30, s75, v210
	v_med3_f32 v26, v31, s75, v210
	v_mov_b32_e32 v25, v165
	v_cvt_pk_fp8_f32 v25, v19, v26
	v_pk_fma_f32 v[28:29], v[98:99], s[22:23], v[2:3] op_sel_hi:[1,0,1]
	v_add_u32_e32 v20, 48, v18
	v_pk_mul_f32 v[28:29], v[28:29], s[24:25] op_sel_hi:[1,0]
	v_ashrrev_i32_e32 v21, 31, v20
	v_med3_f32 v19, v28, s75, v210
	v_med3_f32 v26, v29, s75, v210
	v_lshlrev_b64 v[20:21], 10, v[20:21]
	v_cvt_pk_fp8_f32 v24, v27, v96 op_sel:[0,0,1]
	v_cvt_pk_fp8_f32 v25, v19, v26 op_sel:[0,0,1]
	v_lshl_add_u64 v[20:21], s[12:13], 0, v[20:21]
	v_lshl_add_u64 v[20:21], v[20:21], 0, v[16:17]
	s_nop 1
	v_permlane16_swap_b32_e32 v22, v24
	v_permlane16_swap_b32_e32 v23, v25
	v_lshl_add_u64 v[248:249], v[20:21], 0, v[250:251]
	global_store_dwordx4 v[248:249], v[22:25], off
	s_nop 1
	v_pk_fma_f32 v[22:23], v[94:95], s[22:23], v[14:15] op_sel_hi:[1,0,1]
	v_pk_fma_f32 v[24:25], v[92:93], s[22:23], v[12:13] op_sel_hi:[1,0,1]
	v_pk_mul_f32 v[22:23], v[22:23], s[24:25] op_sel_hi:[1,0]
	v_pk_mul_f32 v[24:25], v[24:25], s[24:25] op_sel_hi:[1,0]
	v_pk_fma_f32 v[28:29], v[88:89], s[22:23], v[8:9] op_sel_hi:[1,0,1]
	v_med3_f32 v19, v24, s75, v210
	v_pk_mul_f32 v[28:29], v[28:29], s[24:25] op_sel_hi:[1,0]
	v_med3_f32 v24, v25, s75, v210
	v_med3_f32 v25, v22, s75, v210
	v_mov_b32_e32 v22, v165
	v_med3_f32 v30, v23, s75, v210
	v_cvt_pk_fp8_f32 v22, v19, v24
	v_med3_f32 v19, v28, s75, v210
	v_med3_f32 v24, v29, s75, v210
	v_mov_b32_e32 v23, v165
	v_cvt_pk_fp8_f32 v23, v19, v24
	v_pk_fma_f32 v[26:27], v[90:91], s[22:23], v[10:11] op_sel_hi:[1,0,1]
	v_cvt_pk_fp8_f32 v22, v25, v30 op_sel:[0,0,1]
	v_pk_mul_f32 v[26:27], v[26:27], s[24:25] op_sel_hi:[1,0]
	v_pk_fma_f32 v[30:31], v[80:81], s[22:23], v[0:1] op_sel_hi:[1,0,1]
	v_med3_f32 v19, v26, s75, v210
	v_med3_f32 v24, v27, s75, v210
	v_cvt_pk_fp8_f32 v23, v19, v24 op_sel:[0,0,1]
	v_pk_fma_f32 v[24:25], v[86:87], s[22:23], v[6:7] op_sel_hi:[1,0,1]
	v_pk_fma_f32 v[26:27], v[84:85], s[22:23], v[4:5] op_sel_hi:[1,0,1]
	v_pk_mul_f32 v[24:25], v[24:25], s[24:25] op_sel_hi:[1,0]
	v_pk_mul_f32 v[26:27], v[26:27], s[24:25] op_sel_hi:[1,0]
	v_pk_mul_f32 v[30:31], v[30:31], s[24:25] op_sel_hi:[1,0]
	v_med3_f32 v19, v26, s75, v210
	v_med3_f32 v26, v27, s75, v210
	v_med3_f32 v27, v24, s75, v210
	v_mov_b32_e32 v24, v165
	v_med3_f32 v80, v25, s75, v210
	v_cvt_pk_fp8_f32 v24, v19, v26
	v_med3_f32 v19, v30, s75, v210
	v_med3_f32 v26, v31, s75, v210
	v_mov_b32_e32 v25, v165
	v_cvt_pk_fp8_f32 v25, v19, v26
	v_pk_fma_f32 v[28:29], v[82:83], s[22:23], v[2:3] op_sel_hi:[1,0,1]
	v_add_u32_e32 v20, 0x80, v18
	v_pk_mul_f32 v[28:29], v[28:29], s[24:25] op_sel_hi:[1,0]
	v_ashrrev_i32_e32 v21, 31, v20
	v_med3_f32 v19, v28, s75, v210
	v_med3_f32 v26, v29, s75, v210
	v_lshlrev_b64 v[20:21], 10, v[20:21]
	v_cvt_pk_fp8_f32 v24, v27, v80 op_sel:[0,0,1]
	v_cvt_pk_fp8_f32 v25, v19, v26 op_sel:[0,0,1]
	v_lshl_add_u64 v[20:21], s[12:13], 0, v[20:21]
	v_lshl_add_u64 v[20:21], v[20:21], 0, v[16:17]
	s_nop 1
	v_permlane16_swap_b32_e32 v22, v24
	v_permlane16_swap_b32_e32 v23, v25
	v_lshl_add_u64 v[248:249], v[20:21], 0, v[250:251]
	global_store_dwordx4 v[248:249], v[22:25], off
	s_nop 1
	v_pk_fma_f32 v[22:23], v[78:79], s[22:23], v[14:15] op_sel_hi:[1,0,1]
	v_pk_fma_f32 v[24:25], v[76:77], s[22:23], v[12:13] op_sel_hi:[1,0,1]
	v_pk_mul_f32 v[22:23], v[22:23], s[24:25] op_sel_hi:[1,0]
	v_pk_mul_f32 v[24:25], v[24:25], s[24:25] op_sel_hi:[1,0]
	v_pk_fma_f32 v[28:29], v[72:73], s[22:23], v[8:9] op_sel_hi:[1,0,1]
	v_med3_f32 v19, v24, s75, v210
	v_pk_mul_f32 v[28:29], v[28:29], s[24:25] op_sel_hi:[1,0]
	v_med3_f32 v24, v25, s75, v210
	v_med3_f32 v25, v22, s75, v210
	v_mov_b32_e32 v22, v165
	v_med3_f32 v30, v23, s75, v210
	v_cvt_pk_fp8_f32 v22, v19, v24
	v_med3_f32 v19, v28, s75, v210
	v_med3_f32 v24, v29, s75, v210
	v_mov_b32_e32 v23, v165
	v_cvt_pk_fp8_f32 v23, v19, v24
	v_pk_fma_f32 v[26:27], v[74:75], s[22:23], v[10:11] op_sel_hi:[1,0,1]
	v_cvt_pk_fp8_f32 v22, v25, v30 op_sel:[0,0,1]
	v_pk_mul_f32 v[26:27], v[26:27], s[24:25] op_sel_hi:[1,0]
	v_pk_fma_f32 v[30:31], v[64:65], s[22:23], v[0:1] op_sel_hi:[1,0,1]
	v_med3_f32 v19, v26, s75, v210
	v_med3_f32 v24, v27, s75, v210
	v_cvt_pk_fp8_f32 v23, v19, v24 op_sel:[0,0,1]
	v_pk_fma_f32 v[24:25], v[70:71], s[22:23], v[6:7] op_sel_hi:[1,0,1]
	v_pk_fma_f32 v[26:27], v[68:69], s[22:23], v[4:5] op_sel_hi:[1,0,1]
	v_pk_mul_f32 v[24:25], v[24:25], s[24:25] op_sel_hi:[1,0]
	v_pk_mul_f32 v[26:27], v[26:27], s[24:25] op_sel_hi:[1,0]
	v_pk_mul_f32 v[30:31], v[30:31], s[24:25] op_sel_hi:[1,0]
	v_med3_f32 v19, v26, s75, v210
	v_med3_f32 v26, v27, s75, v210
	v_med3_f32 v27, v24, s75, v210
	v_mov_b32_e32 v24, v165
	v_med3_f32 v64, v25, s75, v210
	v_cvt_pk_fp8_f32 v24, v19, v26
	v_med3_f32 v19, v30, s75, v210
	v_med3_f32 v26, v31, s75, v210
	v_mov_b32_e32 v25, v165
	v_cvt_pk_fp8_f32 v25, v19, v26
	v_pk_fma_f32 v[28:29], v[66:67], s[22:23], v[2:3] op_sel_hi:[1,0,1]
	v_add_u32_e32 v20, 0x90, v18
	v_pk_mul_f32 v[28:29], v[28:29], s[24:25] op_sel_hi:[1,0]
	v_ashrrev_i32_e32 v21, 31, v20
	v_med3_f32 v19, v28, s75, v210
	v_med3_f32 v26, v29, s75, v210
	v_lshlrev_b64 v[20:21], 10, v[20:21]
	v_cvt_pk_fp8_f32 v24, v27, v64 op_sel:[0,0,1]
	v_cvt_pk_fp8_f32 v25, v19, v26 op_sel:[0,0,1]
	v_lshl_add_u64 v[20:21], s[12:13], 0, v[20:21]
	v_lshl_add_u64 v[20:21], v[20:21], 0, v[16:17]
	s_nop 1
	v_permlane16_swap_b32_e32 v22, v24
	v_permlane16_swap_b32_e32 v23, v25
	v_lshl_add_u64 v[248:249], v[20:21], 0, v[250:251]
	global_store_dwordx4 v[248:249], v[22:25], off
	s_nop 1
	v_pk_fma_f32 v[22:23], v[62:63], s[22:23], v[14:15] op_sel_hi:[1,0,1]
	v_pk_fma_f32 v[24:25], v[60:61], s[22:23], v[12:13] op_sel_hi:[1,0,1]
	v_pk_mul_f32 v[22:23], v[22:23], s[24:25] op_sel_hi:[1,0]
	v_pk_mul_f32 v[24:25], v[24:25], s[24:25] op_sel_hi:[1,0]
	v_pk_fma_f32 v[28:29], v[56:57], s[22:23], v[8:9] op_sel_hi:[1,0,1]
	v_med3_f32 v19, v24, s75, v210
	v_pk_mul_f32 v[28:29], v[28:29], s[24:25] op_sel_hi:[1,0]
	v_med3_f32 v24, v25, s75, v210
	v_med3_f32 v25, v22, s75, v210
	v_mov_b32_e32 v22, v165
	v_med3_f32 v30, v23, s75, v210
	v_cvt_pk_fp8_f32 v22, v19, v24
	v_med3_f32 v19, v28, s75, v210
	v_med3_f32 v24, v29, s75, v210
	v_mov_b32_e32 v23, v165
	v_cvt_pk_fp8_f32 v23, v19, v24
	v_pk_fma_f32 v[26:27], v[58:59], s[22:23], v[10:11] op_sel_hi:[1,0,1]
	v_cvt_pk_fp8_f32 v22, v25, v30 op_sel:[0,0,1]
	v_pk_mul_f32 v[26:27], v[26:27], s[24:25] op_sel_hi:[1,0]
	v_pk_fma_f32 v[30:31], v[48:49], s[22:23], v[0:1] op_sel_hi:[1,0,1]
	v_med3_f32 v19, v26, s75, v210
	v_med3_f32 v24, v27, s75, v210
	v_cvt_pk_fp8_f32 v23, v19, v24 op_sel:[0,0,1]
	v_pk_fma_f32 v[24:25], v[54:55], s[22:23], v[6:7] op_sel_hi:[1,0,1]
	v_pk_fma_f32 v[26:27], v[52:53], s[22:23], v[4:5] op_sel_hi:[1,0,1]
	v_pk_mul_f32 v[24:25], v[24:25], s[24:25] op_sel_hi:[1,0]
	v_pk_mul_f32 v[26:27], v[26:27], s[24:25] op_sel_hi:[1,0]
	v_pk_mul_f32 v[30:31], v[30:31], s[24:25] op_sel_hi:[1,0]
	v_med3_f32 v19, v26, s75, v210
	v_med3_f32 v26, v27, s75, v210
	v_med3_f32 v27, v24, s75, v210
	v_mov_b32_e32 v24, v165
	v_med3_f32 v48, v25, s75, v210
	v_cvt_pk_fp8_f32 v24, v19, v26
	v_med3_f32 v19, v30, s75, v210
	v_med3_f32 v26, v31, s75, v210
	v_mov_b32_e32 v25, v165
	v_cvt_pk_fp8_f32 v25, v19, v26
	v_pk_fma_f32 v[28:29], v[50:51], s[22:23], v[2:3] op_sel_hi:[1,0,1]
	v_add_u32_e32 v20, 0xa0, v18
	v_pk_mul_f32 v[28:29], v[28:29], s[24:25] op_sel_hi:[1,0]
	v_ashrrev_i32_e32 v21, 31, v20
	v_med3_f32 v19, v28, s75, v210
	v_med3_f32 v26, v29, s75, v210
	v_lshlrev_b64 v[20:21], 10, v[20:21]
	v_cvt_pk_fp8_f32 v24, v27, v48 op_sel:[0,0,1]
	v_cvt_pk_fp8_f32 v25, v19, v26 op_sel:[0,0,1]
	v_lshl_add_u64 v[20:21], s[12:13], 0, v[20:21]
	v_pk_fma_f32 v[12:13], v[44:45], s[22:23], v[12:13] op_sel_hi:[1,0,1]
	v_lshl_add_u64 v[20:21], v[20:21], 0, v[16:17]
	v_pk_mul_f32 v[12:13], v[12:13], s[24:25] op_sel_hi:[1,0]
	v_pk_fma_f32 v[8:9], v[40:41], s[22:23], v[8:9] op_sel_hi:[1,0,1]
	s_nop 1
	v_permlane16_swap_b32_e32 v22, v24
	v_permlane16_swap_b32_e32 v23, v25
	v_lshl_add_u64 v[248:249], v[20:21], 0, v[250:251]
	global_store_dwordx4 v[248:249], v[22:25], off
	s_nop 1
	v_pk_mul_f32 v[8:9], v[8:9], s[24:25] op_sel_hi:[1,0]
	v_med3_f32 v20, v12, s75, v210
	v_med3_f32 v13, v13, s75, v210
	v_mov_b32_e32 v12, v165
	v_cvt_pk_fp8_f32 v12, v20, v13
	v_med3_f32 v8, v8, s75, v210
	v_med3_f32 v9, v9, s75, v210
	v_mov_b32_e32 v13, v165
	v_cvt_pk_fp8_f32 v13, v8, v9
	v_pk_fma_f32 v[10:11], v[42:43], s[22:23], v[10:11] op_sel_hi:[1,0,1]
	v_pk_fma_f32 v[4:5], v[36:37], s[22:23], v[4:5] op_sel_hi:[1,0,1]
	v_pk_mul_f32 v[10:11], v[10:11], s[24:25] op_sel_hi:[1,0]
	v_pk_mul_f32 v[4:5], v[4:5], s[24:25] op_sel_hi:[1,0]
	v_med3_f32 v8, v10, s75, v210
	v_med3_f32 v9, v11, s75, v210
	v_pk_fma_f32 v[0:1], v[32:33], s[22:23], v[0:1] op_sel_hi:[1,0,1]
	v_cvt_pk_fp8_f32 v13, v8, v9 op_sel:[0,0,1]
	v_pk_mul_f32 v[0:1], v[0:1], s[24:25] op_sel_hi:[1,0]
	v_med3_f32 v8, v4, s75, v210
	v_med3_f32 v5, v5, s75, v210
	v_mov_b32_e32 v4, v165
	v_cvt_pk_fp8_f32 v4, v8, v5
	v_med3_f32 v0, v0, s75, v210
	v_med3_f32 v1, v1, s75, v210
	v_mov_b32_e32 v5, v165
	v_pk_fma_f32 v[14:15], v[46:47], s[22:23], v[14:15] op_sel_hi:[1,0,1]
	v_cvt_pk_fp8_f32 v5, v0, v1
	v_pk_mul_f32 v[14:15], v[14:15], s[24:25] op_sel_hi:[1,0]
	v_pk_fma_f32 v[6:7], v[38:39], s[22:23], v[6:7] op_sel_hi:[1,0,1]
	v_pk_fma_f32 v[2:3], v[34:35], s[22:23], v[2:3] op_sel_hi:[1,0,1]
	v_add_u32_e32 v18, 0xb0, v18
	v_med3_f32 v14, v14, s75, v210
	v_med3_f32 v15, v15, s75, v210
	v_pk_mul_f32 v[6:7], v[6:7], s[24:25] op_sel_hi:[1,0]
	v_pk_mul_f32 v[2:3], v[2:3], s[24:25] op_sel_hi:[1,0]
	v_ashrrev_i32_e32 v19, 31, v18
	v_cvt_pk_fp8_f32 v12, v14, v15 op_sel:[0,0,1]
	v_med3_f32 v6, v6, s75, v210
	v_med3_f32 v7, v7, s75, v210
	v_med3_f32 v0, v2, s75, v210
	v_med3_f32 v1, v3, s75, v210
	v_lshlrev_b64 v[18:19], 10, v[18:19]
	v_cvt_pk_fp8_f32 v4, v6, v7 op_sel:[0,0,1]
	v_cvt_pk_fp8_f32 v5, v0, v1 op_sel:[0,0,1]
	v_lshl_add_u64 v[0:1], s[12:13], 0, v[18:19]
	v_lshl_add_u64 v[0:1], v[0:1], 0, v[16:17]
	s_mov_b64 s[2:3], -1
	global_store_dwordx2 v[0:1], v[12:13], off
	global_store_dwordx2 v[0:1], v[4:5], off offset:128
	s_cbranch_vccnz .LBB0_1783
	s_andn2_b64 vcc, exec, s[10:11]
	s_cbranch_vccnz .LBB0_1782
	s_barrier
	s_branch .LBB0_1782
